# epilogue de-serialisation: merge-GEMM epilogue issues all 16 gate loads up front instead of 16 load/wait(0) rounds (on top of the w_o and rotary epilogue hoists)
# speedup vs baseline: 1.0033x; 1.0007x over previous
; DI unsigned cvt_pk_bf16(float lo, float hi) { const f32x2_t v = {lo, hi}; return __builtin_bit_cast(unsigned, __builtin_convertvector(v, bf16x2_t)); }
;     DI void operator()(const f32x4 (&acc)[2][2][4][2], const Unit& u, int wr, int wc, int fr, int fq) const {
;         int row0 = u.pm * BM + wr * 64 + fr; asm volatile("" : "+v"(row0));
;         const int col0 = u.pn * BM + wc * 32 + 8 * fq;
; #pragma unroll
;         for (int ai = 0; ai < 2; ++ai)
; #pragma unroll
;             for (int m = 0; m < 4; ++m) { const size_t r = (size_t)(row0 + ai * HALF + m * 16);
; #pragma unroll
;                 for (int bj = 0; bj < 2; ++bj) { const int c = col0 + bj * HALF; f32x4 s0, s1; unpack8f(*(const u32x4*)(G + r * 4096 + 2048 + c), s0, s1);
;                     const f32x4 v0 = acc[ai][bj][m][0] * s0, v1 = acc[ai][bj][m][1] * s1;
;                     u32x4 w; w.x = cvt_pk_bf16(v0[0], v0[1]); w.y = cvt_pk_bf16(v0[2], v0[3]); w.z = cvt_pk_bf16(v1[0], v1[1]); w.w = cvt_pk_bf16(v1[2], v1[3]);
;                     *(u32x4*)(Mg + r * D_ + c) = w; }
;                 asm volatile("" ::: "memory"); }
.LBB0_493:
	v_ashrrev_i32_e32 v153, 31, v148
	v_mov_b32_e32 v152, v148
	v_lshlrev_b64 v[162:163], 13, v[152:153]
	v_lshl_add_u64 v[164:165], s[10:11], 0, v[162:163]
	v_lshl_add_u64 v[166:167], v[164:165], 0, s[16:17]
	v_lshlrev_b64 v[168:169], 1, v[150:151]
	v_lshl_add_u64 v[170:171], v[166:167], 0, v[168:169]
	global_load_dwordx4 v[248:251], v[170:171], off
	v_or_b32_e32 v170, 0x80, v150
	v_ashrrev_i32_e32 v171, 31, v170
	v_lshlrev_b64 v[172:173], 1, v[170:171]
	v_lshl_add_u64 v[174:175], v[166:167], 0, v[172:173]
	global_load_dwordx4 v[244:247], v[174:175], off
	v_add_u32_e32 v152, 16, v148
	v_ashrrev_i32_e32 v153, 31, v152
	v_lshlrev_b64 v[162:163], 13, v[152:153]
	v_lshl_add_u64 v[164:165], s[10:11], 0, v[162:163]
	v_lshl_add_u64 v[166:167], v[164:165], 0, s[16:17]
	v_lshl_add_u64 v[174:175], v[166:167], 0, v[168:169]
	global_load_dwordx4 v[240:243], v[174:175], off
	v_lshl_add_u64 v[174:175], v[166:167], 0, v[172:173]
	global_load_dwordx4 v[236:239], v[174:175], off
	v_add_u32_e32 v152, 32, v148
	v_ashrrev_i32_e32 v153, 31, v152
	v_lshlrev_b64 v[162:163], 13, v[152:153]
	v_lshl_add_u64 v[164:165], s[10:11], 0, v[162:163]
	v_lshl_add_u64 v[166:167], v[164:165], 0, s[16:17]
	v_lshl_add_u64 v[174:175], v[166:167], 0, v[168:169]
	global_load_dwordx4 v[232:235], v[174:175], off
	v_lshl_add_u64 v[174:175], v[166:167], 0, v[172:173]
	global_load_dwordx4 v[228:231], v[174:175], off
	v_add_u32_e32 v152, 48, v148
	v_ashrrev_i32_e32 v153, 31, v152
	v_lshlrev_b64 v[162:163], 13, v[152:153]
	v_lshl_add_u64 v[164:165], s[10:11], 0, v[162:163]
	v_lshl_add_u64 v[166:167], v[164:165], 0, s[16:17]
	v_lshl_add_u64 v[174:175], v[166:167], 0, v[168:169]
	global_load_dwordx4 v[224:227], v[174:175], off
	v_lshl_add_u64 v[174:175], v[166:167], 0, v[172:173]
	global_load_dwordx4 v[220:223], v[174:175], off
	v_add_u32_e32 v152, 0x80, v148
	v_ashrrev_i32_e32 v153, 31, v152
	v_lshlrev_b64 v[162:163], 13, v[152:153]
	v_lshl_add_u64 v[164:165], s[10:11], 0, v[162:163]
	v_lshl_add_u64 v[166:167], v[164:165], 0, s[16:17]
	v_lshl_add_u64 v[174:175], v[166:167], 0, v[168:169]
	global_load_dwordx4 v[216:219], v[174:175], off
	v_lshl_add_u64 v[174:175], v[166:167], 0, v[172:173]
	global_load_dwordx4 v[212:215], v[174:175], off
	v_add_u32_e32 v152, 0x90, v148
	v_ashrrev_i32_e32 v153, 31, v152
	v_lshlrev_b64 v[162:163], 13, v[152:153]
	v_lshl_add_u64 v[164:165], s[10:11], 0, v[162:163]
	v_lshl_add_u64 v[166:167], v[164:165], 0, s[16:17]
	v_lshl_add_u64 v[174:175], v[166:167], 0, v[168:169]
	global_load_dwordx4 v[208:211], v[174:175], off
	v_lshl_add_u64 v[174:175], v[166:167], 0, v[172:173]
	global_load_dwordx4 v[204:207], v[174:175], off
	v_add_u32_e32 v152, 0xa0, v148
	v_ashrrev_i32_e32 v153, 31, v152
	v_lshlrev_b64 v[162:163], 13, v[152:153]
	v_lshl_add_u64 v[164:165], s[10:11], 0, v[162:163]
	v_lshl_add_u64 v[166:167], v[164:165], 0, s[16:17]
	v_lshl_add_u64 v[174:175], v[166:167], 0, v[168:169]
	global_load_dwordx4 v[200:203], v[174:175], off
	v_lshl_add_u64 v[174:175], v[166:167], 0, v[172:173]
	global_load_dwordx4 v[196:199], v[174:175], off
	v_add_u32_e32 v152, 0xb0, v148
	v_ashrrev_i32_e32 v153, 31, v152
	v_lshlrev_b64 v[162:163], 13, v[152:153]
	v_lshl_add_u64 v[164:165], s[10:11], 0, v[162:163]
	v_lshl_add_u64 v[166:167], v[164:165], 0, s[16:17]
	v_lshl_add_u64 v[174:175], v[166:167], 0, v[168:169]
	global_load_dwordx4 v[192:195], v[174:175], off
	v_lshl_add_u64 v[168:169], v[166:167], 0, v[172:173]
	global_load_dwordx4 v[188:191], v[168:169], off
	s_andn2_b64 vcc, exec, s[4:5]
	v_ashrrev_i32_e32 v149, 31, v148
	v_lshlrev_b64 v[2:3], 13, v[148:149]
	v_lshl_add_u64 v[2:3], s[10:11], 0, v[2:3]
	v_lshl_add_u64 v[138:139], v[2:3], 0, s[16:17]
	v_lshlrev_b64 v[2:3], 1, v[150:151]
	v_lshl_add_u64 v[132:133], v[138:139], 0, v[2:3]
	s_nop 0
	v_or_b32_e32 v132, 0x80, v150
	v_lshlrev_b64 v[140:141], 12, v[148:149]
	v_ashrrev_i32_e32 v133, 31, v132
	v_lshl_add_u64 v[140:141], s[12:13], 0, v[140:141]
	v_lshlrev_b64 v[132:133], 1, v[132:133]
	v_lshl_add_u64 v[140:141], v[140:141], 0, v[2:3]
	v_lshl_add_u64 v[138:139], v[138:139], 0, v[132:133]
	s_mov_b64 s[4:5], -1
	s_nop 0
	s_waitcnt vmcnt(15)
	v_lshlrev_b32_e32 v142, 16, v248
	v_and_b32_e32 v143, 0xffff0000, v248
	v_lshlrev_b32_e32 v134, 16, v249
	v_and_b32_e32 v135, 0xffff0000, v249
	v_lshlrev_b32_e32 v150, 16, v250
	v_and_b32_e32 v151, 0xffff0000, v250
	v_lshlrev_b32_e32 v136, 16, v251
	v_and_b32_e32 v137, 0xffff0000, v251
	v_pk_mul_f32 v[130:131], v[130:131], v[134:135]
	v_pk_mul_f32 v[128:129], v[128:129], v[142:143]
	v_pk_mul_f32 v[134:135], v[126:127], v[136:137]
	v_pk_mul_f32 v[126:127], v[124:125], v[150:151]
	v_cvt_pk_bf16_f32 v124, v128, v129
	v_cvt_pk_bf16_f32 v125, v130, v131
	v_cvt_pk_bf16_f32 v126, v126, v127
	v_cvt_pk_bf16_f32 v127, v134, v135
	global_store_dwordx4 v[140:141], v[124:127], off
	s_nop 0
	v_add_u32_e32 v128, 16, v148
	v_ashrrev_i32_e32 v129, 31, v128
	v_lshlrev_b64 v[130:131], 13, v[128:129]
	v_lshl_add_u64 v[130:131], s[10:11], 0, v[130:131]
	v_lshl_add_u64 v[130:131], v[130:131], 0, s[16:17]
	v_lshl_add_u64 v[134:135], v[130:131], 0, v[2:3]
	s_nop 0
	s_waitcnt vmcnt(15)
	v_lshlrev_b32_e32 v136, 16, v244
	v_and_b32_e32 v137, 0xffff0000, v244
	v_lshlrev_b32_e32 v124, 16, v245
	v_and_b32_e32 v125, 0xffff0000, v245
	v_lshlrev_b32_e32 v138, 16, v246
	v_and_b32_e32 v139, 0xffff0000, v246
	v_lshlrev_b32_e32 v126, 16, v247
	v_and_b32_e32 v127, 0xffff0000, v247
	v_pk_mul_f32 v[122:123], v[122:123], v[124:125]
	v_pk_mul_f32 v[120:121], v[120:121], v[136:137]
	v_pk_mul_f32 v[124:125], v[118:119], v[126:127]
	v_pk_mul_f32 v[118:119], v[116:117], v[138:139]
	v_cvt_pk_bf16_f32 v116, v120, v121
	v_cvt_pk_bf16_f32 v117, v122, v123
	v_cvt_pk_bf16_f32 v118, v118, v119
	v_cvt_pk_bf16_f32 v119, v124, v125
	global_store_dwordx4 v[140:141], v[116:119], off offset:256
	s_nop 0
	v_lshlrev_b64 v[120:121], 12, v[128:129]
	v_lshl_add_u64 v[120:121], s[12:13], 0, v[120:121]
	v_lshl_add_u64 v[120:121], v[120:121], 0, v[2:3]
	v_lshl_add_u64 v[122:123], v[130:131], 0, v[132:133]
	s_nop 0
	s_waitcnt vmcnt(15)
; DI unsigned cvt_pk_bf16(float lo, float hi) { const f32x2_t v = {lo, hi}; return __builtin_bit_cast(unsigned, __builtin_convertvector(v, bf16x2_t)); }
;     DI void operator()(const f32x4 (&acc)[2][2][4][2], const Unit& u, int wr, int wc, int fr, int fq) const {
;         int row0 = u.pm * BM + wr * 64 + fr; asm volatile("" : "+v"(row0));
;         const int col0 = u.pn * BM + wc * 32 + 8 * fq;
; #pragma unroll
;         for (int ai = 0; ai < 2; ++ai)
; #pragma unroll
;             for (int m = 0; m < 4; ++m) { const size_t r = (size_t)(row0 + ai * HALF + m * 16);
; #pragma unroll
;                 for (int bj = 0; bj < 2; ++bj) { const int c = col0 + bj * HALF; f32x4 s0, s1; unpack8f(*(const u32x4*)(G + r * 4096 + 2048 + c), s0, s1);
;                     const f32x4 v0 = acc[ai][bj][m][0] * s0, v1 = acc[ai][bj][m][1] * s1;
;                     u32x4 w; w.x = cvt_pk_bf16(v0[0], v0[1]); w.y = cvt_pk_bf16(v0[2], v0[3]); w.z = cvt_pk_bf16(v1[0], v1[1]); w.w = cvt_pk_bf16(v1[2], v1[3]);
;                     *(u32x4*)(Mg + r * D_ + c) = w; }
;                 asm volatile("" ::: "memory"); }
	v_lshlrev_b32_e32 v124, 16, v240
	v_and_b32_e32 v125, 0xffff0000, v240
	v_lshlrev_b32_e32 v116, 16, v241
	v_and_b32_e32 v117, 0xffff0000, v241
	v_lshlrev_b32_e32 v126, 16, v242
	v_and_b32_e32 v127, 0xffff0000, v242
	v_lshlrev_b32_e32 v118, 16, v243
	v_and_b32_e32 v119, 0xffff0000, v243
	v_pk_mul_f32 v[114:115], v[114:115], v[116:117]
	v_pk_mul_f32 v[112:113], v[112:113], v[124:125]
	v_pk_mul_f32 v[116:117], v[110:111], v[118:119]
	v_pk_mul_f32 v[110:111], v[108:109], v[126:127]
	v_cvt_pk_bf16_f32 v108, v112, v113
	v_cvt_pk_bf16_f32 v109, v114, v115
	v_cvt_pk_bf16_f32 v110, v110, v111
	v_cvt_pk_bf16_f32 v111, v116, v117
	global_store_dwordx4 v[120:121], v[108:111], off
	s_nop 0
	v_add_u32_e32 v112, 32, v148
	v_ashrrev_i32_e32 v113, 31, v112
	v_lshlrev_b64 v[114:115], 13, v[112:113]
	v_lshl_add_u64 v[114:115], s[10:11], 0, v[114:115]
	v_lshl_add_u64 v[114:115], v[114:115], 0, s[16:17]
	v_lshl_add_u64 v[116:117], v[114:115], 0, v[2:3]
	s_nop 0
	s_waitcnt vmcnt(15)
	v_lshlrev_b32_e32 v118, 16, v236
	v_and_b32_e32 v119, 0xffff0000, v236
	v_lshlrev_b32_e32 v108, 16, v237
	v_and_b32_e32 v109, 0xffff0000, v237
	v_lshlrev_b32_e32 v122, 16, v238
	v_and_b32_e32 v123, 0xffff0000, v238
	v_lshlrev_b32_e32 v110, 16, v239
	v_and_b32_e32 v111, 0xffff0000, v239
	v_pk_mul_f32 v[106:107], v[106:107], v[108:109]
	v_pk_mul_f32 v[104:105], v[104:105], v[118:119]
	v_pk_mul_f32 v[108:109], v[102:103], v[110:111]
	v_pk_mul_f32 v[102:103], v[100:101], v[122:123]
	v_cvt_pk_bf16_f32 v100, v104, v105
	v_cvt_pk_bf16_f32 v101, v106, v107
	v_cvt_pk_bf16_f32 v102, v102, v103
	v_cvt_pk_bf16_f32 v103, v108, v109
	global_store_dwordx4 v[120:121], v[100:103], off offset:256
	s_nop 0
	v_lshlrev_b64 v[104:105], 12, v[112:113]
	v_lshl_add_u64 v[104:105], s[12:13], 0, v[104:105]
	v_lshl_add_u64 v[104:105], v[104:105], 0, v[2:3]
	v_lshl_add_u64 v[106:107], v[114:115], 0, v[132:133]
	s_nop 0
	s_waitcnt vmcnt(15)
	v_lshlrev_b32_e32 v108, 16, v232
	v_and_b32_e32 v109, 0xffff0000, v232
	v_lshlrev_b32_e32 v100, 16, v233
	v_and_b32_e32 v101, 0xffff0000, v233
	v_lshlrev_b32_e32 v110, 16, v234
	v_and_b32_e32 v111, 0xffff0000, v234
	v_lshlrev_b32_e32 v102, 16, v235
	v_and_b32_e32 v103, 0xffff0000, v235
	v_pk_mul_f32 v[98:99], v[98:99], v[100:101]
	v_pk_mul_f32 v[96:97], v[96:97], v[108:109]
	v_pk_mul_f32 v[100:101], v[94:95], v[102:103]
	v_pk_mul_f32 v[94:95], v[92:93], v[110:111]
	v_cvt_pk_bf16_f32 v92, v96, v97
	v_cvt_pk_bf16_f32 v93, v98, v99
	v_cvt_pk_bf16_f32 v94, v94, v95
	v_cvt_pk_bf16_f32 v95, v100, v101
	global_store_dwordx4 v[104:105], v[92:95], off
	s_nop 0
	v_add_u32_e32 v96, 48, v148
	v_ashrrev_i32_e32 v97, 31, v96
	v_lshlrev_b64 v[98:99], 13, v[96:97]
	v_lshl_add_u64 v[98:99], s[10:11], 0, v[98:99]
	v_lshl_add_u64 v[98:99], v[98:99], 0, s[16:17]
	v_lshl_add_u64 v[100:101], v[98:99], 0, v[2:3]
	s_nop 0
	s_waitcnt vmcnt(15)
	v_lshlrev_b32_e32 v102, 16, v228
	v_and_b32_e32 v103, 0xffff0000, v228
	v_lshlrev_b32_e32 v92, 16, v229
	v_and_b32_e32 v93, 0xffff0000, v229
	v_lshlrev_b32_e32 v106, 16, v230
	v_and_b32_e32 v107, 0xffff0000, v230
	v_lshlrev_b32_e32 v94, 16, v231
	v_and_b32_e32 v95, 0xffff0000, v231
	v_pk_mul_f32 v[90:91], v[90:91], v[92:93]
	v_pk_mul_f32 v[88:89], v[88:89], v[102:103]
	v_pk_mul_f32 v[92:93], v[86:87], v[94:95]
	v_pk_mul_f32 v[86:87], v[84:85], v[106:107]
	v_cvt_pk_bf16_f32 v84, v88, v89
	v_cvt_pk_bf16_f32 v85, v90, v91
	v_cvt_pk_bf16_f32 v86, v86, v87
	v_cvt_pk_bf16_f32 v87, v92, v93
	global_store_dwordx4 v[104:105], v[84:87], off offset:256
	s_nop 0
	v_lshlrev_b64 v[88:89], 12, v[96:97]
	v_lshl_add_u64 v[88:89], s[12:13], 0, v[88:89]
	v_lshl_add_u64 v[88:89], v[88:89], 0, v[2:3]
	v_lshl_add_u64 v[90:91], v[98:99], 0, v[132:133]
	s_nop 0
	s_waitcnt vmcnt(15)
	v_lshlrev_b32_e32 v92, 16, v224
	v_and_b32_e32 v93, 0xffff0000, v224
	v_lshlrev_b32_e32 v84, 16, v225
	v_and_b32_e32 v85, 0xffff0000, v225
	v_lshlrev_b32_e32 v94, 16, v226
	v_and_b32_e32 v95, 0xffff0000, v226
	v_lshlrev_b32_e32 v86, 16, v227
	v_and_b32_e32 v87, 0xffff0000, v227
	v_pk_mul_f32 v[82:83], v[82:83], v[84:85]
	v_pk_mul_f32 v[80:81], v[80:81], v[92:93]
	v_pk_mul_f32 v[84:85], v[78:79], v[86:87]
	v_pk_mul_f32 v[78:79], v[76:77], v[94:95]
	v_cvt_pk_bf16_f32 v76, v80, v81
	v_cvt_pk_bf16_f32 v77, v82, v83
	v_cvt_pk_bf16_f32 v78, v78, v79
	v_cvt_pk_bf16_f32 v79, v84, v85
	global_store_dwordx4 v[88:89], v[76:79], off
	s_nop 0
	v_add_u32_e32 v80, 0x80, v148
	v_ashrrev_i32_e32 v81, 31, v80
	v_lshlrev_b64 v[82:83], 13, v[80:81]
	v_lshl_add_u64 v[82:83], s[10:11], 0, v[82:83]
	v_lshl_add_u64 v[82:83], v[82:83], 0, s[16:17]
	v_lshl_add_u64 v[84:85], v[82:83], 0, v[2:3]
	s_nop 0
	s_waitcnt vmcnt(15)
	v_lshlrev_b32_e32 v86, 16, v220
	v_and_b32_e32 v87, 0xffff0000, v220
	v_lshlrev_b32_e32 v76, 16, v221
	v_and_b32_e32 v77, 0xffff0000, v221
	v_lshlrev_b32_e32 v90, 16, v222
	v_and_b32_e32 v91, 0xffff0000, v222
	v_lshlrev_b32_e32 v78, 16, v223
	v_and_b32_e32 v79, 0xffff0000, v223
	v_pk_mul_f32 v[74:75], v[74:75], v[76:77]
	v_pk_mul_f32 v[72:73], v[72:73], v[86:87]
	v_pk_mul_f32 v[76:77], v[70:71], v[78:79]
	v_pk_mul_f32 v[70:71], v[68:69], v[90:91]
	v_cvt_pk_bf16_f32 v68, v72, v73
	v_cvt_pk_bf16_f32 v69, v74, v75
	v_cvt_pk_bf16_f32 v70, v70, v71
	v_cvt_pk_bf16_f32 v71, v76, v77
	global_store_dwordx4 v[88:89], v[68:71], off offset:256
	s_nop 0
	v_lshlrev_b64 v[72:73], 12, v[80:81]
	v_lshl_add_u64 v[72:73], s[12:13], 0, v[72:73]
	v_lshl_add_u64 v[72:73], v[72:73], 0, v[2:3]
	v_lshl_add_u64 v[74:75], v[82:83], 0, v[132:133]
	s_nop 0
	s_waitcnt vmcnt(15)
; DI unsigned cvt_pk_bf16(float lo, float hi) { const f32x2_t v = {lo, hi}; return __builtin_bit_cast(unsigned, __builtin_convertvector(v, bf16x2_t)); }
; #define PG8_BAR __builtin_amdgcn_s_barrier()
;     DI int nt(const Unit& u) const { return (u.aux & 8) ? PLED / 64 : ((u.aux & 4) ? (D_ / 2) / 64 : D_ / 64); }
; template <class Epi, class Sched, bool ALIGN_EPI, bool FP8 = false>
; DI void gemm_phase(LAS unsigned char* lds, const Gemm g, const Sched& S, const Epi& E) {
;     ...
;         if (!has_next) break;
; #pragma unroll
;         for (int a = 0; a < 2; ++a)
; #pragma unroll
;             for (int b = 0; b < 2; ++b)
; #pragma unroll
;                 for (int m = 0; m < 4; ++m)
; #pragma unroll
;                     for (int n = 0; n < 2; ++n) acc[a][b][m][n] = (f32x4){0.f, 0.f, 0.f, 0.f};
;         cur = nxt; cA = nA; cB = nB; ++ui;
;         if constexpr (sched_vark<Sched>::value) nt = S.nt(cur);
;         if constexpr (ALIGN_EPI) { if (wr == 1) PG8_BAR; }
;     DI void operator()(const f32x4 (&acc)[2][2][4][2], const Unit& u, int wr, int wc, int fr, int fq) const {
;         int row0 = u.pm * BM + wr * 64 + fr; asm volatile("" : "+v"(row0));
;         const int col0 = u.pn * BM + wc * 32 + 8 * fq;
; #pragma unroll
;         for (int ai = 0; ai < 2; ++ai)
; #pragma unroll
;             for (int m = 0; m < 4; ++m) { const size_t r = (size_t)(row0 + ai * HALF + m * 16);
; #pragma unroll
;                 for (int bj = 0; bj < 2; ++bj) { const int c = col0 + bj * HALF; f32x4 s0, s1; unpack8f(*(const u32x4*)(G + r * 4096 + 2048 + c), s0, s1);
;                     const f32x4 v0 = acc[ai][bj][m][0] * s0, v1 = acc[ai][bj][m][1] * s1;
;                     u32x4 w; w.x = cvt_pk_bf16(v0[0], v0[1]); w.y = cvt_pk_bf16(v0[2], v0[3]); w.z = cvt_pk_bf16(v1[0], v1[1]); w.w = cvt_pk_bf16(v1[2], v1[3]);
;                     *(u32x4*)(Mg + r * D_ + c) = w; }
;                 asm volatile("" ::: "memory"); }
	v_lshlrev_b32_e32 v76, 16, v216
	v_and_b32_e32 v77, 0xffff0000, v216
	v_lshlrev_b32_e32 v68, 16, v217
	v_and_b32_e32 v69, 0xffff0000, v217
	v_lshlrev_b32_e32 v78, 16, v218
	v_and_b32_e32 v79, 0xffff0000, v218
	v_lshlrev_b32_e32 v70, 16, v219
	v_and_b32_e32 v71, 0xffff0000, v219
	v_pk_mul_f32 v[66:67], v[66:67], v[68:69]
	v_pk_mul_f32 v[64:65], v[64:65], v[76:77]
	v_pk_mul_f32 v[68:69], v[62:63], v[70:71]
	v_pk_mul_f32 v[62:63], v[60:61], v[78:79]
	v_cvt_pk_bf16_f32 v60, v64, v65
	v_cvt_pk_bf16_f32 v61, v66, v67
	v_cvt_pk_bf16_f32 v62, v62, v63
	v_cvt_pk_bf16_f32 v63, v68, v69
	global_store_dwordx4 v[72:73], v[60:63], off
	s_nop 0
	v_add_u32_e32 v64, 0x90, v148
	v_ashrrev_i32_e32 v65, 31, v64
	v_lshlrev_b64 v[66:67], 13, v[64:65]
	v_lshl_add_u64 v[66:67], s[10:11], 0, v[66:67]
	v_lshl_add_u64 v[66:67], v[66:67], 0, s[16:17]
	v_lshl_add_u64 v[68:69], v[66:67], 0, v[2:3]
	s_nop 0
	s_waitcnt vmcnt(15)
	v_lshlrev_b32_e32 v70, 16, v212
	v_and_b32_e32 v71, 0xffff0000, v212
	v_lshlrev_b32_e32 v60, 16, v213
	v_and_b32_e32 v61, 0xffff0000, v213
	v_lshlrev_b32_e32 v74, 16, v214
	v_and_b32_e32 v75, 0xffff0000, v214
	v_lshlrev_b32_e32 v62, 16, v215
	v_and_b32_e32 v63, 0xffff0000, v215
	v_pk_mul_f32 v[58:59], v[58:59], v[60:61]
	v_pk_mul_f32 v[56:57], v[56:57], v[70:71]
	v_pk_mul_f32 v[60:61], v[54:55], v[62:63]
	v_pk_mul_f32 v[54:55], v[52:53], v[74:75]
	v_cvt_pk_bf16_f32 v52, v56, v57
	v_cvt_pk_bf16_f32 v53, v58, v59
	v_cvt_pk_bf16_f32 v54, v54, v55
	v_cvt_pk_bf16_f32 v55, v60, v61
	global_store_dwordx4 v[72:73], v[52:55], off offset:256
	s_nop 0
	v_lshlrev_b64 v[56:57], 12, v[64:65]
	v_lshl_add_u64 v[56:57], s[12:13], 0, v[56:57]
	v_lshl_add_u64 v[56:57], v[56:57], 0, v[2:3]
	v_lshl_add_u64 v[58:59], v[66:67], 0, v[132:133]
	s_nop 0
	s_waitcnt vmcnt(15)
	v_lshlrev_b32_e32 v60, 16, v208
	v_and_b32_e32 v61, 0xffff0000, v208
	v_lshlrev_b32_e32 v52, 16, v209
	v_and_b32_e32 v53, 0xffff0000, v209
	v_lshlrev_b32_e32 v62, 16, v210
	v_and_b32_e32 v63, 0xffff0000, v210
	v_lshlrev_b32_e32 v54, 16, v211
	v_and_b32_e32 v55, 0xffff0000, v211
	v_pk_mul_f32 v[50:51], v[50:51], v[52:53]
	v_pk_mul_f32 v[48:49], v[48:49], v[60:61]
	v_pk_mul_f32 v[52:53], v[46:47], v[54:55]
	v_pk_mul_f32 v[46:47], v[44:45], v[62:63]
	v_cvt_pk_bf16_f32 v44, v48, v49
	v_cvt_pk_bf16_f32 v45, v50, v51
	v_cvt_pk_bf16_f32 v46, v46, v47
	v_cvt_pk_bf16_f32 v47, v52, v53
	global_store_dwordx4 v[56:57], v[44:47], off
	s_nop 0
	v_add_u32_e32 v48, 0xa0, v148
	v_ashrrev_i32_e32 v49, 31, v48
	v_lshlrev_b64 v[50:51], 13, v[48:49]
	v_lshl_add_u64 v[50:51], s[10:11], 0, v[50:51]
	v_lshl_add_u64 v[50:51], v[50:51], 0, s[16:17]
	v_lshl_add_u64 v[52:53], v[50:51], 0, v[2:3]
	s_nop 0
	s_waitcnt vmcnt(15)
	v_lshlrev_b32_e32 v54, 16, v204
	v_and_b32_e32 v55, 0xffff0000, v204
	v_lshlrev_b32_e32 v44, 16, v205
	v_and_b32_e32 v45, 0xffff0000, v205
	v_lshlrev_b32_e32 v58, 16, v206
	v_and_b32_e32 v59, 0xffff0000, v206
	v_lshlrev_b32_e32 v46, 16, v207
	v_and_b32_e32 v47, 0xffff0000, v207
	v_pk_mul_f32 v[42:43], v[42:43], v[44:45]
	v_pk_mul_f32 v[40:41], v[40:41], v[54:55]
	v_pk_mul_f32 v[44:45], v[38:39], v[46:47]
	v_pk_mul_f32 v[38:39], v[36:37], v[58:59]
	v_cvt_pk_bf16_f32 v36, v40, v41
	v_cvt_pk_bf16_f32 v37, v42, v43
	v_cvt_pk_bf16_f32 v38, v38, v39
	v_cvt_pk_bf16_f32 v39, v44, v45
	global_store_dwordx4 v[56:57], v[36:39], off offset:256
	s_nop 0
	v_lshlrev_b64 v[40:41], 12, v[48:49]
	v_lshl_add_u64 v[40:41], s[12:13], 0, v[40:41]
	v_lshl_add_u64 v[40:41], v[40:41], 0, v[2:3]
	v_lshl_add_u64 v[42:43], v[50:51], 0, v[132:133]
	s_nop 0
	s_waitcnt vmcnt(15)
	v_lshlrev_b32_e32 v44, 16, v200
	v_and_b32_e32 v45, 0xffff0000, v200
	v_lshlrev_b32_e32 v36, 16, v201
	v_and_b32_e32 v37, 0xffff0000, v201
	v_lshlrev_b32_e32 v46, 16, v202
	v_and_b32_e32 v47, 0xffff0000, v202
	v_lshlrev_b32_e32 v38, 16, v203
	v_and_b32_e32 v39, 0xffff0000, v203
	v_pk_mul_f32 v[34:35], v[34:35], v[36:37]
	v_pk_mul_f32 v[32:33], v[32:33], v[44:45]
	v_pk_mul_f32 v[36:37], v[30:31], v[38:39]
	v_pk_mul_f32 v[30:31], v[28:29], v[46:47]
	v_cvt_pk_bf16_f32 v28, v32, v33
	v_cvt_pk_bf16_f32 v29, v34, v35
	v_cvt_pk_bf16_f32 v30, v30, v31
	v_cvt_pk_bf16_f32 v31, v36, v37
	global_store_dwordx4 v[40:41], v[28:31], off
	s_nop 0
	v_add_u32_e32 v32, 0xb0, v148
	v_ashrrev_i32_e32 v33, 31, v32
	v_lshlrev_b64 v[34:35], 13, v[32:33]
	v_lshl_add_u64 v[34:35], s[10:11], 0, v[34:35]
	v_lshl_add_u64 v[34:35], v[34:35], 0, s[16:17]
	v_lshl_add_u64 v[36:37], v[34:35], 0, v[2:3]
	s_nop 0
	s_waitcnt vmcnt(15)
	v_lshlrev_b32_e32 v38, 16, v196
	v_and_b32_e32 v39, 0xffff0000, v196
	v_lshlrev_b32_e32 v28, 16, v197
	v_and_b32_e32 v29, 0xffff0000, v197
	v_lshlrev_b32_e32 v42, 16, v198
	v_and_b32_e32 v43, 0xffff0000, v198
	v_lshlrev_b32_e32 v30, 16, v199
	v_and_b32_e32 v31, 0xffff0000, v199
	v_pk_mul_f32 v[26:27], v[26:27], v[28:29]
	v_pk_mul_f32 v[24:25], v[24:25], v[38:39]
	v_pk_mul_f32 v[28:29], v[22:23], v[30:31]
	v_pk_mul_f32 v[22:23], v[20:21], v[42:43]
	v_cvt_pk_bf16_f32 v20, v24, v25
	v_cvt_pk_bf16_f32 v21, v26, v27
	v_cvt_pk_bf16_f32 v22, v22, v23
	v_cvt_pk_bf16_f32 v23, v28, v29
	global_store_dwordx4 v[40:41], v[20:23], off offset:256
	s_nop 0
	v_lshlrev_b64 v[24:25], 12, v[32:33]
	v_lshl_add_u64 v[24:25], s[12:13], 0, v[24:25]
	v_lshl_add_u64 v[24:25], v[24:25], 0, v[2:3]
	v_lshl_add_u64 v[2:3], v[34:35], 0, v[132:133]
	s_nop 0
	s_waitcnt vmcnt(15)
	v_lshlrev_b32_e32 v26, 16, v192
	v_and_b32_e32 v27, 0xffff0000, v192
	v_lshlrev_b32_e32 v20, 16, v193
	v_and_b32_e32 v21, 0xffff0000, v193
	v_lshlrev_b32_e32 v28, 16, v194
	v_and_b32_e32 v29, 0xffff0000, v194
	v_lshlrev_b32_e32 v22, 16, v195
	v_and_b32_e32 v23, 0xffff0000, v195
	v_pk_mul_f32 v[18:19], v[18:19], v[20:21]
	v_pk_mul_f32 v[16:17], v[16:17], v[26:27]
	v_pk_mul_f32 v[20:21], v[14:15], v[22:23]
	v_pk_mul_f32 v[14:15], v[12:13], v[28:29]
	v_cvt_pk_bf16_f32 v12, v16, v17
	v_cvt_pk_bf16_f32 v13, v18, v19
	v_cvt_pk_bf16_f32 v14, v14, v15
	v_cvt_pk_bf16_f32 v15, v20, v21
	global_store_dwordx4 v[24:25], v[12:15], off
	s_nop 0
	s_nop 0
	s_waitcnt vmcnt(15)
	v_lshlrev_b32_e32 v2, 16, v188
	v_and_b32_e32 v3, 0xffff0000, v188
	v_lshlrev_b32_e32 v12, 16, v189
	v_and_b32_e32 v13, 0xffff0000, v189
	v_lshlrev_b32_e32 v16, 16, v190
	v_and_b32_e32 v17, 0xffff0000, v190
	v_lshlrev_b32_e32 v14, 16, v191
	v_and_b32_e32 v15, 0xffff0000, v191
	v_pk_mul_f32 v[10:11], v[10:11], v[12:13]
	v_pk_mul_f32 v[2:3], v[8:9], v[2:3]
	v_pk_mul_f32 v[6:7], v[6:7], v[14:15]
	v_pk_mul_f32 v[4:5], v[4:5], v[16:17]
	v_cvt_pk_bf16_f32 v2, v2, v3
	v_cvt_pk_bf16_f32 v3, v10, v11
	v_cvt_pk_bf16_f32 v4, v4, v5
	v_cvt_pk_bf16_f32 v5, v6, v7
	global_store_dwordx4 v[24:25], v[2:5], off offset:256
	s_cbranch_vccnz .LBB0_480
	s_andn2_b64 vcc, exec, s[8:9]
	s_cbranch_vccnz .LBB0_479
	s_barrier
	s_branch .LBB0_479
